# DSA indexer top-k: bit-count loop rewritten (v_cmp to SGPR pair + carry add per element, DPP/permlane16 half-wave sum instead of 5 ds_bpermute)
# speedup vs baseline: 1.0027x; 1.0027x over previous
.LBB0_2738:
	v_lshl_or_b32 v14, 1, v13, v7
	v_mov_b32_e32 v15, 0
	v_cmp_ge_u32_e64 s[28:29], v148, v14
	v_cmp_ge_u32_e64 s[30:31], v149, v14
	v_cmp_ge_u32_e64 s[34:35], v147, v14
	v_addc_co_u32_e64 v15, vcc, 0, v15, s[28:29]
	v_cmp_ge_u32_e64 s[28:29], v145, v14
	v_addc_co_u32_e64 v15, vcc, 0, v15, s[30:31]
	v_cmp_ge_u32_e64 s[30:31], v146, v14
	v_addc_co_u32_e64 v15, vcc, 0, v15, s[34:35]
	v_cmp_ge_u32_e64 s[34:35], v144, v14
	v_addc_co_u32_e64 v15, vcc, 0, v15, s[28:29]
	v_cmp_ge_u32_e64 s[28:29], v143, v14
	v_addc_co_u32_e64 v15, vcc, 0, v15, s[30:31]
	v_cmp_ge_u32_e64 s[30:31], v142, v14
	v_addc_co_u32_e64 v15, vcc, 0, v15, s[34:35]
	v_cmp_ge_u32_e64 s[34:35], v140, v14
	v_addc_co_u32_e64 v15, vcc, 0, v15, s[28:29]
	v_cmp_ge_u32_e64 s[28:29], v139, v14
	v_addc_co_u32_e64 v15, vcc, 0, v15, s[30:31]
	v_cmp_ge_u32_e64 s[30:31], v138, v14
	v_addc_co_u32_e64 v15, vcc, 0, v15, s[34:35]
	v_cmp_ge_u32_e64 s[34:35], v137, v14
	v_addc_co_u32_e64 v15, vcc, 0, v15, s[28:29]
	v_cmp_ge_u32_e64 s[28:29], v136, v14
	v_addc_co_u32_e64 v15, vcc, 0, v15, s[30:31]
	v_cmp_ge_u32_e64 s[30:31], v135, v14
	v_addc_co_u32_e64 v15, vcc, 0, v15, s[34:35]
	v_cmp_ge_u32_e64 s[34:35], v134, v14
	v_addc_co_u32_e64 v15, vcc, 0, v15, s[28:29]
	v_cmp_ge_u32_e64 s[28:29], v133, v14
	v_addc_co_u32_e64 v15, vcc, 0, v15, s[30:31]
	v_cmp_ge_u32_e64 s[30:31], v132, v14
	v_addc_co_u32_e64 v15, vcc, 0, v15, s[34:35]
	v_cmp_ge_u32_e64 s[34:35], v131, v14
	v_addc_co_u32_e64 v15, vcc, 0, v15, s[28:29]
	v_cmp_ge_u32_e64 s[28:29], v130, v14
	v_addc_co_u32_e64 v15, vcc, 0, v15, s[30:31]
	v_cmp_ge_u32_e64 s[30:31], v129, v14
	v_addc_co_u32_e64 v15, vcc, 0, v15, s[34:35]
	v_cmp_ge_u32_e64 s[34:35], v128, v14
	v_addc_co_u32_e64 v15, vcc, 0, v15, s[28:29]
	v_cmp_ge_u32_e64 s[28:29], v127, v14
	v_addc_co_u32_e64 v15, vcc, 0, v15, s[30:31]
	v_cmp_ge_u32_e64 s[30:31], v126, v14
	v_addc_co_u32_e64 v15, vcc, 0, v15, s[34:35]
	v_cmp_ge_u32_e64 s[34:35], v125, v14
	v_addc_co_u32_e64 v15, vcc, 0, v15, s[28:29]
	v_cmp_ge_u32_e64 s[28:29], v124, v14
	v_addc_co_u32_e64 v15, vcc, 0, v15, s[30:31]
	v_cmp_ge_u32_e64 s[30:31], v123, v14
	v_addc_co_u32_e64 v15, vcc, 0, v15, s[34:35]
	v_cmp_ge_u32_e64 s[34:35], v122, v14
	v_addc_co_u32_e64 v15, vcc, 0, v15, s[28:29]
	v_cmp_ge_u32_e64 s[28:29], v121, v14
	v_addc_co_u32_e64 v15, vcc, 0, v15, s[30:31]
	v_cmp_ge_u32_e64 s[30:31], v120, v14
	v_addc_co_u32_e64 v15, vcc, 0, v15, s[34:35]
	v_cmp_ge_u32_e64 s[34:35], v119, v14
	v_addc_co_u32_e64 v15, vcc, 0, v15, s[28:29]
	v_cmp_ge_u32_e64 s[28:29], v118, v14
	v_addc_co_u32_e64 v15, vcc, 0, v15, s[30:31]
	v_cmp_ge_u32_e64 s[30:31], v116, v14
	v_addc_co_u32_e64 v15, vcc, 0, v15, s[34:35]
	v_cmp_ge_u32_e64 s[34:35], v114, v14
	v_addc_co_u32_e64 v15, vcc, 0, v15, s[28:29]
	v_cmp_ge_u32_e64 s[28:29], v112, v14
	v_addc_co_u32_e64 v15, vcc, 0, v15, s[30:31]
	v_cmp_ge_u32_e64 s[30:31], v111, v14
	v_addc_co_u32_e64 v15, vcc, 0, v15, s[34:35]
	v_cmp_ge_u32_e64 s[34:35], v110, v14
	v_addc_co_u32_e64 v15, vcc, 0, v15, s[28:29]
	v_cmp_ge_u32_e64 s[28:29], v109, v14
	v_addc_co_u32_e64 v15, vcc, 0, v15, s[30:31]
	v_cmp_ge_u32_e64 s[30:31], v108, v14
	v_addc_co_u32_e64 v15, vcc, 0, v15, s[34:35]
	v_cmp_ge_u32_e64 s[34:35], v106, v14
	v_addc_co_u32_e64 v15, vcc, 0, v15, s[28:29]
	v_cmp_ge_u32_e64 s[28:29], v105, v14
	v_addc_co_u32_e64 v15, vcc, 0, v15, s[30:31]
	v_cmp_ge_u32_e64 s[30:31], v104, v14
	v_addc_co_u32_e64 v15, vcc, 0, v15, s[34:35]
	v_cmp_ge_u32_e64 s[34:35], v102, v14
	v_addc_co_u32_e64 v15, vcc, 0, v15, s[28:29]
	v_cmp_ge_u32_e64 s[28:29], v101, v14
	v_addc_co_u32_e64 v15, vcc, 0, v15, s[30:31]
	v_cmp_ge_u32_e64 s[30:31], v99, v14
	v_addc_co_u32_e64 v15, vcc, 0, v15, s[34:35]
	v_cmp_ge_u32_e64 s[34:35], v98, v14
	v_addc_co_u32_e64 v15, vcc, 0, v15, s[28:29]
	v_cmp_ge_u32_e64 s[28:29], v96, v14
	v_addc_co_u32_e64 v15, vcc, 0, v15, s[30:31]
	v_cmp_ge_u32_e64 s[30:31], v95, v14
	v_addc_co_u32_e64 v15, vcc, 0, v15, s[34:35]
	v_cmp_ge_u32_e64 s[34:35], v94, v14
	v_addc_co_u32_e64 v15, vcc, 0, v15, s[28:29]
	v_cmp_ge_u32_e64 s[28:29], v93, v14
	v_addc_co_u32_e64 v15, vcc, 0, v15, s[30:31]
	v_cmp_ge_u32_e64 s[30:31], v92, v14
	v_addc_co_u32_e64 v15, vcc, 0, v15, s[34:35]
	v_cmp_ge_u32_e64 s[34:35], v91, v14
	v_addc_co_u32_e64 v15, vcc, 0, v15, s[28:29]
	v_cmp_ge_u32_e64 s[28:29], v90, v14
	v_addc_co_u32_e64 v15, vcc, 0, v15, s[30:31]
	v_cmp_ge_u32_e64 s[30:31], v89, v14
	v_addc_co_u32_e64 v15, vcc, 0, v15, s[34:35]
	v_cmp_ge_u32_e64 s[34:35], v88, v14
	v_addc_co_u32_e64 v15, vcc, 0, v15, s[28:29]
	v_cmp_ge_u32_e64 s[28:29], v85, v14
	v_addc_co_u32_e64 v15, vcc, 0, v15, s[30:31]
	v_cmp_ge_u32_e64 s[30:31], v84, v14
	v_addc_co_u32_e64 v15, vcc, 0, v15, s[34:35]
	v_cmp_ge_u32_e64 s[34:35], v103, v14
	v_addc_co_u32_e64 v15, vcc, 0, v15, s[28:29]
	v_cmp_ge_u32_e64 s[28:29], v100, v14
	v_addc_co_u32_e64 v15, vcc, 0, v15, s[30:31]
	v_cmp_ge_u32_e64 s[30:31], v97, v14
	v_addc_co_u32_e64 v15, vcc, 0, v15, s[34:35]
	v_cmp_ge_u32_e64 s[34:35], v107, v14
	v_addc_co_u32_e64 v15, vcc, 0, v15, s[28:29]
	v_cmp_ge_u32_e64 s[28:29], v117, v14
	v_addc_co_u32_e64 v15, vcc, 0, v15, s[30:31]
	v_cmp_ge_u32_e64 s[30:31], v115, v14
	v_addc_co_u32_e64 v15, vcc, 0, v15, s[34:35]
	v_cmp_ge_u32_e64 s[34:35], v113, v14
	v_addc_co_u32_e64 v15, vcc, 0, v15, s[28:29]
	v_cmp_ge_u32_e64 s[28:29], v6, v14
	v_addc_co_u32_e64 v15, vcc, 0, v15, s[30:31]
	v_addc_co_u32_e64 v15, vcc, 0, v15, s[34:35]
	v_addc_co_u32_e64 v15, vcc, 0, v15, s[28:29]
	s_nop 1
	v_add_u32_dpp v15, v15, v15 quad_perm:[1,0,3,2] row_mask:0xf bank_mask:0xf
	s_nop 1
	v_add_u32_dpp v15, v15, v15 quad_perm:[2,3,0,1] row_mask:0xf bank_mask:0xf
	s_nop 1
	v_add_u32_dpp v15, v15, v15 row_half_mirror row_mask:0xf bank_mask:0xf
	s_nop 1
	v_add_u32_dpp v15, v15, v15 row_mirror row_mask:0xf bank_mask:0xf
	v_mov_b32_e32 v16, v15
	s_nop 1
	v_permlane16_swap_b32_e32 v15, v16
	v_add_u32_e32 v15, v15, v16


	v_cmp_gt_i32_e32 vcc, s4, v15
	s_or_b64 vcc, s[2:3], vcc
	v_cmp_eq_u32_e64 s[0:1], s4, v15
	v_cndmask_b32_e32 v7, v14, v7, vcc
	v_cndmask_b32_e64 v15, 0, 1, s[2:3]
	v_cndmask_b32_e64 v14, 0, 1, s[0:1]
	v_cndmask_b32_e32 v14, v14, v15, vcc
	v_and_b32_e32 v14, 1, v14
	v_cmp_ne_u32_e32 vcc, 0, v14
	s_cmp_eq_u64 vcc, exec
	s_cselect_b64 s[0:1], -1, 0
	v_subrev_co_u32_e32 v13, vcc, 1, v13
	s_or_b64 s[0:1], s[0:1], vcc
	v_cmp_eq_u32_e64 s[2:3], 1, v14
	s_andn2_b64 vcc, exec, s[0:1]
	s_cbranch_vccnz .LBB0_2738
	v_cmp_gt_u32_e64 s[2:3], v98, v7
	v_cmp_gt_u32_e64 s[30:31], v147, v7
	v_cmp_gt_u32_e64 s[28:29], v145, v7
	v_writelane_b32 v254, s2, 32
	v_cndmask_b32_e64 v13, 0, 1, s[30:31]
	v_cndmask_b32_e64 v14, 0, 1, s[28:29]
	v_writelane_b32 v254, s3, 33
	v_cndmask_b32_e64 v31, 0, 1, s[2:3]
	v_cmp_gt_u32_e64 s[2:3], v95, v7
	v_lshlrev_b16_e32 v13, 2, v13
	v_lshlrev_b16_e32 v14, 3, v14
	v_writelane_b32 v254, s2, 34
	v_cmp_gt_u32_e64 s[34:35], v148, v7
	v_or_b32_e32 v13, v14, v13
	v_writelane_b32 v254, s3, 35
	v_cndmask_b32_e64 v32, 0, 1, s[2:3]
	v_cmp_gt_u32_e64 s[2:3], v93, v7
	v_cndmask_b32_e64 v14, 0, 1, s[34:35]
	v_cmp_gt_u32_e64 s[36:37], v149, v7
	v_writelane_b32 v254, s2, 36
	v_lshlrev_b16_e32 v14, 1, v14
	v_cndmask_b32_e64 v15, 0, 1, s[36:37]
	v_writelane_b32 v254, s3, 37
	v_cndmask_b32_e64 v33, 0, 1, s[2:3]
	v_cmp_gt_u32_e64 s[2:3], v91, v7
	v_or_b32_e32 v14, v15, v14
	v_cmp_gt_u32_e64 s[18:19], v143, v7
	v_writelane_b32 v254, s2, 38
	v_cmp_gt_u32_e64 s[16:17], v142, v7
	v_bitop3_b16 v13, v14, v13, 3 bitop3:0xec
	v_writelane_b32 v254, s3, 39
	v_cndmask_b32_e64 v34, 0, 1, s[2:3]
	v_cmp_gt_u32_e64 s[2:3], v89, v7
	v_cndmask_b32_e64 v14, 0, 1, s[18:19]
	v_cndmask_b32_e64 v15, 0, 1, s[16:17]
	v_writelane_b32 v254, s2, 40
	v_lshlrev_b16_e32 v14, 2, v14
	v_lshlrev_b16_e32 v15, 3, v15
	v_writelane_b32 v254, s3, 41
	v_cndmask_b32_e64 v35, 0, 1, s[2:3]
	v_cmp_gt_u32_e64 s[2:3], v85, v7
	v_cmp_gt_u32_e64 s[22:23], v144, v7
	v_or_b32_e32 v14, v15, v14
	v_writelane_b32 v254, s2, 42
	v_cndmask_b32_e64 v15, 0, 1, s[22:23]
	v_cmp_gt_u32_e64 s[26:27], v146, v7
	v_writelane_b32 v254, s3, 43
	v_cndmask_b32_e64 v36, 0, 1, s[2:3]
	v_cmp_gt_u32_e64 s[2:3], v103, v7
	v_lshlrev_b16_e32 v15, 1, v15
	v_cndmask_b32_e64 v16, 0, 1, s[26:27]
	v_writelane_b32 v254, s2, 44
	v_or_b32_e32 v15, v16, v15
	v_bitop3_b16 v14, v15, v14, 3 bitop3:0xec
	v_writelane_b32 v254, s3, 45
	v_cndmask_b32_e64 v37, 0, 1, s[2:3]
	v_cmp_gt_u32_e64 s[2:3], v97, v7
	v_lshlrev_b16_e32 v14, 4, v14
	v_cmp_gt_u32_e64 s[10:11], v138, v7
	v_writelane_b32 v254, s2, 46
	v_cmp_gt_u32_e64 s[8:9], v136, v7
	v_cmp_gt_u32_e64 s[96:97], v132, v7
	v_writelane_b32 v254, s3, 47
	v_cndmask_b32_e64 v38, 0, 1, s[2:3]
	v_cmp_gt_u32_e64 s[2:3], v117, v7
	v_cmp_gt_u32_e64 s[88:89], v128, v7
	v_cmp_gt_u32_e64 s[80:81], v124, v7
	v_writelane_b32 v254, s2, 48
	v_cmp_gt_u32_e64 s[72:73], v120, v7
	v_cmp_gt_u32_e64 s[66:67], v114, v7
	v_cmp_gt_u32_e64 s[56:57], v109, v7
	v_cmp_gt_u32_e64 s[48:49], v104, v7
	v_writelane_b32 v254, s3, 49
	v_cndmask_b32_e64 v39, 0, 1, s[2:3]
	v_cmp_gt_u32_e64 s[2:3], v113, v7
	v_bitop3_b16 v13, v13, v14, 15 bitop3:0xec
	v_cndmask_b32_e64 v14, 0, 1, s[10:11]
	v_cndmask_b32_e64 v15, 0, 1, s[8:9]
	v_cndmask_b32_e64 v17, 0, 1, s[96:97]
	v_cndmask_b32_e64 v19, 0, 1, s[88:89]
	v_cndmask_b32_e64 v21, 0, 1, s[80:81]
	v_cndmask_b32_e64 v23, 0, 1, s[72:73]
	v_cndmask_b32_e64 v25, 0, 1, s[66:67]
	v_cndmask_b32_e64 v27, 0, 1, s[56:57]
	v_cndmask_b32_e64 v29, 0, 1, s[48:49]
	v_writelane_b32 v254, s2, 50
	v_cmp_gt_u32_e64 s[20:21], v139, v7
	v_cmp_gt_u32_e64 s[14:15], v137, v7
	v_cmp_gt_u32_e64 s[6:7], v133, v7
	v_cmp_gt_u32_e64 s[94:95], v129, v7
	v_cmp_gt_u32_e64 s[86:87], v125, v7
	v_cmp_gt_u32_e64 s[78:79], v121, v7
	v_cmp_gt_u32_e64 s[70:71], v116, v7
	v_cmp_gt_u32_e64 s[62:63], v110, v7
	v_cmp_gt_u32_e64 s[54:55], v105, v7
	v_writelane_b32 v254, s3, 51
	v_cndmask_b32_e64 v40, 0, 1, s[2:3]
	v_addc_co_u32_e64 v14, s[2:3], 0, v14, s[20:21]
	v_addc_co_u32_e64 v15, s[2:3], 0, v15, s[14:15]
	v_addc_co_u32_e64 v17, s[2:3], 0, v17, s[6:7]
	v_addc_co_u32_e64 v19, s[2:3], 0, v19, s[94:95]
	v_addc_co_u32_e64 v21, s[2:3], 0, v21, s[86:87]
	v_addc_co_u32_e64 v23, s[2:3], 0, v23, s[78:79]
	v_addc_co_u32_e64 v25, s[2:3], 0, v25, s[70:71]
	v_addc_co_u32_e64 v27, s[2:3], 0, v27, s[62:63]
	v_addc_co_u32_e64 v29, s[2:3], 0, v29, s[54:55]
	v_cmp_gt_u32_e64 s[2:3], v99, v7
	v_cmp_gt_u32_e64 s[44:45], v134, v7
	v_and_b32_e32 v13, 0xff, v13
	v_writelane_b32 v254, s2, 52
	v_cndmask_b32_e64 v16, 0, 1, s[44:45]
	v_bcnt_u32_b32 v13, v13, 0
	v_writelane_b32 v254, s3, 53
	v_addc_co_u32_e64 v31, s[2:3], 0, v31, s[2:3]
	v_cmp_gt_u32_e64 s[2:3], v94, v7
	v_cmp_gt_u32_e64 s[24:25], v140, v7
	v_cmp_gt_u32_e64 s[12:13], v135, v7
	v_writelane_b32 v254, s2, 54
	v_cmp_gt_u32_e64 s[90:91], v130, v7
	v_cmp_gt_u32_e64 s[82:83], v126, v7
	v_writelane_b32 v254, s3, 55
	v_addc_co_u32_e64 v33, s[2:3], 0, v33, s[2:3]
	v_cmp_gt_u32_e64 s[2:3], v90, v7
	v_cmp_gt_u32_e64 s[74:75], v122, v7
	v_cmp_gt_u32_e64 s[42:43], v118, v7
	v_writelane_b32 v254, s2, 56
	v_cmp_gt_u32_e64 s[60:61], v111, v7
	v_cmp_gt_u32_e64 s[52:53], v106, v7
	v_writelane_b32 v254, s3, 57
	v_addc_co_u32_e64 v35, s[2:3], 0, v35, s[2:3]
	v_cmp_gt_u32_e64 s[2:3], v84, v7
	v_cmp_gt_u32_e64 s[0:1], v101, v7
	v_cndmask_b32_e64 v18, 0, 1, s[90:91]
	v_writelane_b32 v254, s2, 58
	v_cndmask_b32_e64 v20, 0, 1, s[82:83]
	v_cndmask_b32_e64 v22, 0, 1, s[74:75]
	v_writelane_b32 v254, s3, 59
	v_addc_co_u32_e64 v37, s[2:3], 0, v37, s[2:3]
	v_cmp_gt_u32_e64 s[2:3], v107, v7
	v_cndmask_b32_e64 v24, 0, 1, s[42:43]
	v_cndmask_b32_e64 v26, 0, 1, s[60:61]
	v_writelane_b32 v254, s2, 60
	v_cndmask_b32_e64 v28, 0, 1, s[52:53]
	v_cndmask_b32_e64 v30, 0, 1, s[0:1]
	v_writelane_b32 v254, s3, 61
	v_addc_co_u32_e64 v39, s[2:3], 0, v39, s[2:3]
	v_addc_co_u32_e64 v13, s[2:3], v14, v13, s[24:25]
	v_addc_co_u32_e64 v14, s[2:3], v15, v16, s[12:13]
	v_cmp_gt_u32_e64 s[2:3], v131, v7
	v_cmp_gt_u32_e64 s[92:93], v127, v7
	v_cmp_gt_u32_e64 s[84:85], v123, v7
	v_cmp_gt_u32_e64 s[76:77], v119, v7
	v_cmp_gt_u32_e64 s[40:41], v112, v7
	v_cmp_gt_u32_e64 s[58:59], v108, v7
	v_cmp_gt_u32_e64 s[50:51], v102, v7
	v_addc_co_u32_e64 v15, s[4:5], v17, v18, s[2:3]
	v_addc_co_u32_e64 v16, s[4:5], v19, v20, s[92:93]
	v_addc_co_u32_e64 v17, s[4:5], v21, v22, s[84:85]
	v_addc_co_u32_e64 v18, s[4:5], v23, v24, s[76:77]
	v_addc_co_u32_e64 v19, s[4:5], v25, v26, s[40:41]
	v_addc_co_u32_e64 v20, s[4:5], v27, v28, s[58:59]
	v_addc_co_u32_e64 v21, s[4:5], v29, v30, s[50:51]
	v_cmp_gt_u32_e64 s[4:5], v96, v7
	v_add_u32_e32 v15, v15, v16
	v_add_u32_e32 v16, v19, v20
	v_writelane_b32 v254, s4, 62
	v_add3_u32 v13, v13, v14, v15
	v_add3_u32 v14, v17, v18, v16
	v_writelane_b32 v254, s5, 63
	v_addc_co_u32_e64 v22, s[4:5], v31, v32, s[4:5]
	v_cmp_gt_u32_e64 s[4:5], v92, v7
	v_add_u32_e32 v19, v21, v22
	v_cmp_eq_u32_e64 s[38:39], v149, v7
	v_writelane_b32 v255, s4, 0
	s_nop 1
	v_writelane_b32 v255, s5, 1
	v_addc_co_u32_e64 v23, s[4:5], v33, v34, s[4:5]
	v_cmp_gt_u32_e64 s[4:5], v88, v7
	s_nop 1
	v_writelane_b32 v255, s4, 2
	s_nop 1
	v_writelane_b32 v255, s5, 3
	v_addc_co_u32_e64 v24, s[4:5], v35, v36, s[4:5]
	v_cmp_gt_u32_e64 s[4:5], v100, v7
	v_add_u32_e32 v20, v23, v24
	s_nop 0
	v_writelane_b32 v255, s4, 4
	s_nop 1
	v_writelane_b32 v255, s5, 5
	v_addc_co_u32_e64 v25, s[4:5], v37, v38, s[4:5]
	v_cmp_gt_u32_e64 s[4:5], v115, v7
	s_nop 1
	v_writelane_b32 v255, s4, 6
	s_nop 1
	v_writelane_b32 v255, s5, 7
	v_addc_co_u32_e64 v26, s[4:5], v39, v40, s[4:5]
	v_cmp_gt_u32_e64 s[4:5], v6, v7
	s_nop 1
	v_writelane_b32 v255, s4, 8
	s_nop 1
	v_writelane_b32 v255, s5, 9
	v_addc_co_u32_e64 v15, s[4:5], v25, v26, s[4:5]
	v_add3_u32 v15, v19, v20, v15
	v_add3_u32 v13, v13, v14, v15
	ds_bpermute_b32 v8, v8, v13
	v_cmp_eq_u32_e64 s[4:5], 0, v141
	s_waitcnt lgkmcnt(0)
	v_add_u32_e32 v8, v8, v13
	ds_bpermute_b32 v9, v9, v8
	s_waitcnt lgkmcnt(0)
	v_add_u32_e32 v8, v8, v9
	ds_bpermute_b32 v9, v10, v8
	v_mov_b32_e32 v10, s39
	s_waitcnt lgkmcnt(0)
	v_add_u32_e32 v8, v8, v9
	ds_bpermute_b32 v9, v11, v8
	v_mov_b32_e32 v11, s38
	v_cndmask_b32_e64 v10, v10, v11, s[4:5]
	s_waitcnt lgkmcnt(0)
	v_add_u32_e32 v8, v8, v9
	ds_bpermute_b32 v9, v12, v8
	s_waitcnt lgkmcnt(0)
	v_add_u32_e32 v8, v8, v9
	v_sub_u32_e32 v9, 0x100, v8
	v_lshlrev_b32_e64 v8, v1, -1
	v_bitop3_b32 v11, v10, v8, v10 bitop3:0x30
	v_bcnt_u32_b32 v11, v11, 0
	v_cmp_lt_i32_e32 vcc, v11, v9
	s_and_b64 s[38:39], s[38:39], vcc
	s_or_b64 s[38:39], s[36:37], s[38:39]
	v_cndmask_b32_e64 v11, 0, 1, s[38:39]
	v_cmp_ne_u32_e32 vcc, 0, v11
	v_not_b32_e32 v8, v8
	s_nop 0
	v_mov_b32_e32 v11, vcc_hi
	v_mov_b32_e32 v12, vcc_lo
	v_cndmask_b32_e64 v11, v11, v12, s[4:5]
	s_and_saveexec_b64 s[36:37], s[38:39]
	s_cbranch_execz .LBB0_2741
	v_and_b32_e32 v12, v11, v8
	v_bcnt_u32_b32 v12, v12, 0
	v_lshlrev_b32_e32 v86, 1, v12
	v_lshl_add_u64 v[12:13], v[4:5], 0, v[86:87]
	global_store_short v[12:13], v1, off

.LBB0_2894:
	v_lshl_or_b32 v14, 1, v13, v7
	v_mov_b32_e32 v15, 0
	v_cmp_ge_u32_e64 s[28:29], v148, v14
	v_cmp_ge_u32_e64 s[30:31], v149, v14
	v_cmp_ge_u32_e64 s[34:35], v147, v14
	v_addc_co_u32_e64 v15, vcc, 0, v15, s[28:29]
	v_cmp_ge_u32_e64 s[28:29], v145, v14
	v_addc_co_u32_e64 v15, vcc, 0, v15, s[30:31]
	v_cmp_ge_u32_e64 s[30:31], v146, v14
	v_addc_co_u32_e64 v15, vcc, 0, v15, s[34:35]
	v_cmp_ge_u32_e64 s[34:35], v144, v14
	v_addc_co_u32_e64 v15, vcc, 0, v15, s[28:29]
	v_cmp_ge_u32_e64 s[28:29], v143, v14
	v_addc_co_u32_e64 v15, vcc, 0, v15, s[30:31]
	v_cmp_ge_u32_e64 s[30:31], v142, v14
	v_addc_co_u32_e64 v15, vcc, 0, v15, s[34:35]
	v_cmp_ge_u32_e64 s[34:35], v140, v14
	v_addc_co_u32_e64 v15, vcc, 0, v15, s[28:29]
	v_cmp_ge_u32_e64 s[28:29], v139, v14
	v_addc_co_u32_e64 v15, vcc, 0, v15, s[30:31]
	v_cmp_ge_u32_e64 s[30:31], v138, v14
	v_addc_co_u32_e64 v15, vcc, 0, v15, s[34:35]
	v_cmp_ge_u32_e64 s[34:35], v137, v14
	v_addc_co_u32_e64 v15, vcc, 0, v15, s[28:29]
	v_cmp_ge_u32_e64 s[28:29], v136, v14
	v_addc_co_u32_e64 v15, vcc, 0, v15, s[30:31]
	v_cmp_ge_u32_e64 s[30:31], v135, v14
	v_addc_co_u32_e64 v15, vcc, 0, v15, s[34:35]
	v_cmp_ge_u32_e64 s[34:35], v134, v14
	v_addc_co_u32_e64 v15, vcc, 0, v15, s[28:29]
	v_cmp_ge_u32_e64 s[28:29], v133, v14
	v_addc_co_u32_e64 v15, vcc, 0, v15, s[30:31]
	v_cmp_ge_u32_e64 s[30:31], v132, v14
	v_addc_co_u32_e64 v15, vcc, 0, v15, s[34:35]
	v_cmp_ge_u32_e64 s[34:35], v131, v14
	v_addc_co_u32_e64 v15, vcc, 0, v15, s[28:29]
	v_cmp_ge_u32_e64 s[28:29], v130, v14
	v_addc_co_u32_e64 v15, vcc, 0, v15, s[30:31]
	v_cmp_ge_u32_e64 s[30:31], v129, v14
	v_addc_co_u32_e64 v15, vcc, 0, v15, s[34:35]
	v_cmp_ge_u32_e64 s[34:35], v128, v14
	v_addc_co_u32_e64 v15, vcc, 0, v15, s[28:29]
	v_cmp_ge_u32_e64 s[28:29], v127, v14
	v_addc_co_u32_e64 v15, vcc, 0, v15, s[30:31]
	v_cmp_ge_u32_e64 s[30:31], v126, v14
	v_addc_co_u32_e64 v15, vcc, 0, v15, s[34:35]
	v_cmp_ge_u32_e64 s[34:35], v125, v14
	v_addc_co_u32_e64 v15, vcc, 0, v15, s[28:29]
	v_cmp_ge_u32_e64 s[28:29], v124, v14
	v_addc_co_u32_e64 v15, vcc, 0, v15, s[30:31]
	v_cmp_ge_u32_e64 s[30:31], v123, v14
	v_addc_co_u32_e64 v15, vcc, 0, v15, s[34:35]
	v_cmp_ge_u32_e64 s[34:35], v122, v14
	v_addc_co_u32_e64 v15, vcc, 0, v15, s[28:29]
	v_cmp_ge_u32_e64 s[28:29], v121, v14
	v_addc_co_u32_e64 v15, vcc, 0, v15, s[30:31]
	v_cmp_ge_u32_e64 s[30:31], v120, v14
	v_addc_co_u32_e64 v15, vcc, 0, v15, s[34:35]
	v_cmp_ge_u32_e64 s[34:35], v119, v14
	v_addc_co_u32_e64 v15, vcc, 0, v15, s[28:29]
	v_cmp_ge_u32_e64 s[28:29], v118, v14
	v_addc_co_u32_e64 v15, vcc, 0, v15, s[30:31]
	v_cmp_ge_u32_e64 s[30:31], v116, v14
	v_addc_co_u32_e64 v15, vcc, 0, v15, s[34:35]
	v_cmp_ge_u32_e64 s[34:35], v114, v14
	v_addc_co_u32_e64 v15, vcc, 0, v15, s[28:29]
	v_cmp_ge_u32_e64 s[28:29], v112, v14
	v_addc_co_u32_e64 v15, vcc, 0, v15, s[30:31]
	v_cmp_ge_u32_e64 s[30:31], v111, v14
	v_addc_co_u32_e64 v15, vcc, 0, v15, s[34:35]
	v_cmp_ge_u32_e64 s[34:35], v110, v14
	v_addc_co_u32_e64 v15, vcc, 0, v15, s[28:29]
	v_cmp_ge_u32_e64 s[28:29], v109, v14
	v_addc_co_u32_e64 v15, vcc, 0, v15, s[30:31]
	v_cmp_ge_u32_e64 s[30:31], v108, v14
	v_addc_co_u32_e64 v15, vcc, 0, v15, s[34:35]
	v_cmp_ge_u32_e64 s[34:35], v106, v14
	v_addc_co_u32_e64 v15, vcc, 0, v15, s[28:29]
	v_cmp_ge_u32_e64 s[28:29], v105, v14
	v_addc_co_u32_e64 v15, vcc, 0, v15, s[30:31]
	v_cmp_ge_u32_e64 s[30:31], v104, v14
	v_addc_co_u32_e64 v15, vcc, 0, v15, s[34:35]
	v_cmp_ge_u32_e64 s[34:35], v102, v14
	v_addc_co_u32_e64 v15, vcc, 0, v15, s[28:29]
	v_cmp_ge_u32_e64 s[28:29], v101, v14
	v_addc_co_u32_e64 v15, vcc, 0, v15, s[30:31]
	v_cmp_ge_u32_e64 s[30:31], v99, v14
	v_addc_co_u32_e64 v15, vcc, 0, v15, s[34:35]
	v_cmp_ge_u32_e64 s[34:35], v98, v14
	v_addc_co_u32_e64 v15, vcc, 0, v15, s[28:29]
	v_cmp_ge_u32_e64 s[28:29], v96, v14
	v_addc_co_u32_e64 v15, vcc, 0, v15, s[30:31]
	v_cmp_ge_u32_e64 s[30:31], v95, v14
	v_addc_co_u32_e64 v15, vcc, 0, v15, s[34:35]
	v_cmp_ge_u32_e64 s[34:35], v94, v14
	v_addc_co_u32_e64 v15, vcc, 0, v15, s[28:29]
	v_cmp_ge_u32_e64 s[28:29], v93, v14
	v_addc_co_u32_e64 v15, vcc, 0, v15, s[30:31]
	v_cmp_ge_u32_e64 s[30:31], v92, v14
	v_addc_co_u32_e64 v15, vcc, 0, v15, s[34:35]
	v_cmp_ge_u32_e64 s[34:35], v91, v14
	v_addc_co_u32_e64 v15, vcc, 0, v15, s[28:29]
	v_cmp_ge_u32_e64 s[28:29], v90, v14
	v_addc_co_u32_e64 v15, vcc, 0, v15, s[30:31]
	v_cmp_ge_u32_e64 s[30:31], v89, v14
	v_addc_co_u32_e64 v15, vcc, 0, v15, s[34:35]
	v_cmp_ge_u32_e64 s[34:35], v88, v14
	v_addc_co_u32_e64 v15, vcc, 0, v15, s[28:29]
	v_cmp_ge_u32_e64 s[28:29], v85, v14
	v_addc_co_u32_e64 v15, vcc, 0, v15, s[30:31]
	v_cmp_ge_u32_e64 s[30:31], v84, v14
	v_addc_co_u32_e64 v15, vcc, 0, v15, s[34:35]
	v_cmp_ge_u32_e64 s[34:35], v103, v14
	v_addc_co_u32_e64 v15, vcc, 0, v15, s[28:29]
	v_cmp_ge_u32_e64 s[28:29], v100, v14
	v_addc_co_u32_e64 v15, vcc, 0, v15, s[30:31]
	v_cmp_ge_u32_e64 s[30:31], v97, v14
	v_addc_co_u32_e64 v15, vcc, 0, v15, s[34:35]
	v_cmp_ge_u32_e64 s[34:35], v107, v14
	v_addc_co_u32_e64 v15, vcc, 0, v15, s[28:29]
	v_cmp_ge_u32_e64 s[28:29], v117, v14
	v_addc_co_u32_e64 v15, vcc, 0, v15, s[30:31]
	v_cmp_ge_u32_e64 s[30:31], v115, v14
	v_addc_co_u32_e64 v15, vcc, 0, v15, s[34:35]
	v_cmp_ge_u32_e64 s[34:35], v113, v14
	v_addc_co_u32_e64 v15, vcc, 0, v15, s[28:29]
	v_cmp_ge_u32_e64 s[28:29], v6, v14
	v_addc_co_u32_e64 v15, vcc, 0, v15, s[30:31]
	v_addc_co_u32_e64 v15, vcc, 0, v15, s[34:35]
	v_addc_co_u32_e64 v15, vcc, 0, v15, s[28:29]
	s_nop 1
	v_add_u32_dpp v15, v15, v15 quad_perm:[1,0,3,2] row_mask:0xf bank_mask:0xf
	s_nop 1
	v_add_u32_dpp v15, v15, v15 quad_perm:[2,3,0,1] row_mask:0xf bank_mask:0xf
	s_nop 1
	v_add_u32_dpp v15, v15, v15 row_half_mirror row_mask:0xf bank_mask:0xf
	s_nop 1
	v_add_u32_dpp v15, v15, v15 row_mirror row_mask:0xf bank_mask:0xf
	v_mov_b32_e32 v16, v15
	s_nop 1
	v_permlane16_swap_b32_e32 v15, v16
	v_add_u32_e32 v15, v15, v16


	v_cmp_gt_i32_e32 vcc, s4, v15
	s_or_b64 vcc, s[2:3], vcc
	v_cmp_eq_u32_e64 s[0:1], s4, v15
	v_cndmask_b32_e32 v7, v14, v7, vcc
	v_cndmask_b32_e64 v15, 0, 1, s[2:3]
	v_cndmask_b32_e64 v14, 0, 1, s[0:1]
	v_cndmask_b32_e32 v14, v14, v15, vcc
	v_and_b32_e32 v14, 1, v14
	v_cmp_ne_u32_e32 vcc, 0, v14
	s_cmp_eq_u64 vcc, exec
	s_cselect_b64 s[0:1], -1, 0
	v_subrev_co_u32_e32 v13, vcc, 1, v13
	s_or_b64 s[0:1], s[0:1], vcc
	v_cmp_eq_u32_e64 s[2:3], 1, v14
	s_andn2_b64 vcc, exec, s[0:1]
	s_cbranch_vccnz .LBB0_2894
	v_cmp_gt_u32_e64 s[2:3], v98, v7
	v_cmp_gt_u32_e64 s[30:31], v147, v7
	v_cmp_gt_u32_e64 s[28:29], v145, v7
	v_writelane_b32 v255, s2, 0
	v_cndmask_b32_e64 v13, 0, 1, s[30:31]
	v_cndmask_b32_e64 v14, 0, 1, s[28:29]
	v_writelane_b32 v255, s3, 1
	v_cndmask_b32_e64 v31, 0, 1, s[2:3]
	v_cmp_gt_u32_e64 s[2:3], v95, v7
	v_lshlrev_b16_e32 v13, 2, v13
	v_lshlrev_b16_e32 v14, 3, v14
	v_writelane_b32 v254, s2, 56
	v_cmp_gt_u32_e64 s[34:35], v148, v7
	v_or_b32_e32 v13, v14, v13
	v_writelane_b32 v254, s3, 57
	v_cndmask_b32_e64 v32, 0, 1, s[2:3]
	v_cmp_gt_u32_e64 s[2:3], v93, v7
	v_cndmask_b32_e64 v14, 0, 1, s[34:35]
	v_cmp_gt_u32_e64 s[36:37], v149, v7
	v_writelane_b32 v255, s2, 2
	v_lshlrev_b16_e32 v14, 1, v14
	v_cndmask_b32_e64 v15, 0, 1, s[36:37]
	v_writelane_b32 v255, s3, 3
	v_cndmask_b32_e64 v33, 0, 1, s[2:3]
	v_cmp_gt_u32_e64 s[2:3], v91, v7
	v_or_b32_e32 v14, v15, v14
	v_cmp_gt_u32_e64 s[18:19], v143, v7
	v_writelane_b32 v254, s2, 58
	v_cmp_gt_u32_e64 s[16:17], v142, v7
	v_bitop3_b16 v13, v14, v13, 3 bitop3:0xec
	v_writelane_b32 v254, s3, 59
	v_cndmask_b32_e64 v34, 0, 1, s[2:3]
	v_cmp_gt_u32_e64 s[2:3], v89, v7
	v_cndmask_b32_e64 v14, 0, 1, s[18:19]
	v_cndmask_b32_e64 v15, 0, 1, s[16:17]
	v_writelane_b32 v255, s2, 4
	v_lshlrev_b16_e32 v14, 2, v14
	v_lshlrev_b16_e32 v15, 3, v15
	v_writelane_b32 v255, s3, 5
	v_cndmask_b32_e64 v35, 0, 1, s[2:3]
	v_cmp_gt_u32_e64 s[2:3], v85, v7
	v_cmp_gt_u32_e64 s[22:23], v144, v7
	v_or_b32_e32 v14, v15, v14
	v_writelane_b32 v254, s2, 60
	v_cndmask_b32_e64 v15, 0, 1, s[22:23]
	v_cmp_gt_u32_e64 s[26:27], v146, v7
	v_writelane_b32 v254, s3, 61
	v_cndmask_b32_e64 v36, 0, 1, s[2:3]
	v_cmp_gt_u32_e64 s[2:3], v103, v7
	v_lshlrev_b16_e32 v15, 1, v15
	v_cndmask_b32_e64 v16, 0, 1, s[26:27]
	v_writelane_b32 v255, s2, 6
	v_or_b32_e32 v15, v16, v15
	v_bitop3_b16 v14, v15, v14, 3 bitop3:0xec
	v_writelane_b32 v255, s3, 7
	v_cndmask_b32_e64 v37, 0, 1, s[2:3]
	v_cmp_gt_u32_e64 s[2:3], v97, v7
	v_lshlrev_b16_e32 v14, 4, v14
	v_cmp_gt_u32_e64 s[10:11], v138, v7
	v_writelane_b32 v255, s2, 8
	v_cmp_gt_u32_e64 s[8:9], v136, v7
	v_cmp_gt_u32_e64 s[96:97], v132, v7
	v_writelane_b32 v255, s3, 9
	v_cndmask_b32_e64 v38, 0, 1, s[2:3]
	v_cmp_gt_u32_e64 s[2:3], v117, v7
	v_cmp_gt_u32_e64 s[88:89], v128, v7
	v_cmp_gt_u32_e64 s[80:81], v124, v7
	v_writelane_b32 v254, s2, 30
	v_cmp_gt_u32_e64 s[72:73], v120, v7
	v_cmp_gt_u32_e64 s[66:67], v114, v7
	v_cmp_gt_u32_e64 s[56:57], v109, v7
	v_cmp_gt_u32_e64 s[48:49], v104, v7
	v_writelane_b32 v254, s3, 31
	v_cndmask_b32_e64 v39, 0, 1, s[2:3]
	v_cmp_gt_u32_e64 s[2:3], v113, v7
	v_bitop3_b16 v13, v13, v14, 15 bitop3:0xec
	v_cndmask_b32_e64 v14, 0, 1, s[10:11]
	v_cndmask_b32_e64 v15, 0, 1, s[8:9]
	v_cndmask_b32_e64 v17, 0, 1, s[96:97]
	v_cndmask_b32_e64 v19, 0, 1, s[88:89]
	v_cndmask_b32_e64 v21, 0, 1, s[80:81]
	v_cndmask_b32_e64 v23, 0, 1, s[72:73]
	v_cndmask_b32_e64 v25, 0, 1, s[66:67]
	v_cndmask_b32_e64 v27, 0, 1, s[56:57]
	v_cndmask_b32_e64 v29, 0, 1, s[48:49]
	v_writelane_b32 v254, s2, 11
	v_cmp_gt_u32_e64 s[20:21], v139, v7
	v_cmp_gt_u32_e64 s[14:15], v137, v7
	v_cmp_gt_u32_e64 s[6:7], v133, v7
	v_cmp_gt_u32_e64 s[94:95], v129, v7
	v_cmp_gt_u32_e64 s[86:87], v125, v7
	v_cmp_gt_u32_e64 s[78:79], v121, v7
	v_cmp_gt_u32_e64 s[70:71], v116, v7
	v_cmp_gt_u32_e64 s[62:63], v110, v7
	v_cmp_gt_u32_e64 s[54:55], v105, v7
	v_writelane_b32 v254, s3, 12
	v_cndmask_b32_e64 v40, 0, 1, s[2:3]
	v_addc_co_u32_e64 v14, s[2:3], 0, v14, s[20:21]
	v_addc_co_u32_e64 v15, s[2:3], 0, v15, s[14:15]
	v_addc_co_u32_e64 v17, s[2:3], 0, v17, s[6:7]
	v_addc_co_u32_e64 v19, s[2:3], 0, v19, s[94:95]
	v_addc_co_u32_e64 v21, s[2:3], 0, v21, s[86:87]
	v_addc_co_u32_e64 v23, s[2:3], 0, v23, s[78:79]
	v_addc_co_u32_e64 v25, s[2:3], 0, v25, s[70:71]
	v_addc_co_u32_e64 v27, s[2:3], 0, v27, s[62:63]
	v_addc_co_u32_e64 v29, s[2:3], 0, v29, s[54:55]
	v_cmp_gt_u32_e64 s[2:3], v99, v7
	v_cmp_gt_u32_e64 s[44:45], v134, v7
	v_and_b32_e32 v13, 0xff, v13
	v_writelane_b32 v254, s2, 54
	v_cndmask_b32_e64 v16, 0, 1, s[44:45]
	v_bcnt_u32_b32 v13, v13, 0
	v_writelane_b32 v254, s3, 55
	v_addc_co_u32_e64 v31, s[2:3], 0, v31, s[2:3]
	v_cmp_gt_u32_e64 s[2:3], v94, v7
	v_cmp_gt_u32_e64 s[24:25], v140, v7
	v_cmp_gt_u32_e64 s[12:13], v135, v7
	v_writelane_b32 v254, s2, 36
	v_cmp_gt_u32_e64 s[90:91], v130, v7
	v_cmp_gt_u32_e64 s[82:83], v126, v7
	v_writelane_b32 v254, s3, 37
	v_addc_co_u32_e64 v33, s[2:3], 0, v33, s[2:3]
	v_cmp_gt_u32_e64 s[2:3], v90, v7
	v_cmp_gt_u32_e64 s[74:75], v122, v7
	v_cmp_gt_u32_e64 s[42:43], v118, v7
	v_writelane_b32 v254, s2, 40
	v_cmp_gt_u32_e64 s[60:61], v111, v7
	v_cmp_gt_u32_e64 s[52:53], v106, v7
	v_writelane_b32 v254, s3, 41
	v_addc_co_u32_e64 v35, s[2:3], 0, v35, s[2:3]
	v_cmp_gt_u32_e64 s[2:3], v84, v7
	v_cmp_gt_u32_e64 s[0:1], v101, v7
	v_cndmask_b32_e64 v18, 0, 1, s[90:91]
	v_writelane_b32 v254, s2, 44
	v_cndmask_b32_e64 v20, 0, 1, s[82:83]
	v_cndmask_b32_e64 v22, 0, 1, s[74:75]
	v_writelane_b32 v254, s3, 45
	v_addc_co_u32_e64 v37, s[2:3], 0, v37, s[2:3]
	v_cmp_gt_u32_e64 s[2:3], v107, v7
	v_cndmask_b32_e64 v24, 0, 1, s[42:43]
	v_cndmask_b32_e64 v26, 0, 1, s[60:61]
	v_writelane_b32 v254, s2, 48
	v_cndmask_b32_e64 v28, 0, 1, s[52:53]
	v_cndmask_b32_e64 v30, 0, 1, s[0:1]
	v_writelane_b32 v254, s3, 49
	v_addc_co_u32_e64 v39, s[2:3], 0, v39, s[2:3]
	v_addc_co_u32_e64 v13, s[2:3], v14, v13, s[24:25]
	v_addc_co_u32_e64 v14, s[2:3], v15, v16, s[12:13]
	v_cmp_gt_u32_e64 s[2:3], v131, v7
	v_cmp_gt_u32_e64 s[92:93], v127, v7
	v_cmp_gt_u32_e64 s[84:85], v123, v7
	v_cmp_gt_u32_e64 s[76:77], v119, v7
	v_cmp_gt_u32_e64 s[40:41], v112, v7
	v_cmp_gt_u32_e64 s[58:59], v108, v7
	v_cmp_gt_u32_e64 s[50:51], v102, v7
	v_addc_co_u32_e64 v15, s[4:5], v17, v18, s[2:3]
	v_addc_co_u32_e64 v16, s[4:5], v19, v20, s[92:93]
	v_addc_co_u32_e64 v17, s[4:5], v21, v22, s[84:85]
	v_addc_co_u32_e64 v18, s[4:5], v23, v24, s[76:77]
	v_addc_co_u32_e64 v19, s[4:5], v25, v26, s[40:41]
	v_addc_co_u32_e64 v20, s[4:5], v27, v28, s[58:59]
	v_addc_co_u32_e64 v21, s[4:5], v29, v30, s[50:51]
	v_cmp_gt_u32_e64 s[4:5], v96, v7
	v_add_u32_e32 v15, v15, v16
	v_add_u32_e32 v16, v19, v20
	v_writelane_b32 v254, s4, 34
	v_add3_u32 v13, v13, v14, v15
	v_add3_u32 v14, v17, v18, v16
	v_writelane_b32 v254, s5, 35
	v_addc_co_u32_e64 v22, s[4:5], v31, v32, s[4:5]
	v_cmp_gt_u32_e64 s[4:5], v92, v7
	v_add_u32_e32 v19, v21, v22
	v_cmp_eq_u32_e64 s[38:39], v149, v7
	v_writelane_b32 v254, s4, 38
	s_nop 1
	v_writelane_b32 v254, s5, 39
	v_addc_co_u32_e64 v23, s[4:5], v33, v34, s[4:5]
	v_cmp_gt_u32_e64 s[4:5], v88, v7
	s_nop 1
	v_writelane_b32 v254, s4, 42
	s_nop 1
	v_writelane_b32 v254, s5, 43
	v_addc_co_u32_e64 v24, s[4:5], v35, v36, s[4:5]
	v_cmp_gt_u32_e64 s[4:5], v100, v7
	v_add_u32_e32 v20, v23, v24
	s_nop 0
	v_writelane_b32 v254, s4, 46
	s_nop 1
	v_writelane_b32 v254, s5, 47
	v_addc_co_u32_e64 v25, s[4:5], v37, v38, s[4:5]
	v_cmp_gt_u32_e64 s[4:5], v115, v7
	s_nop 1
	v_writelane_b32 v254, s4, 50
	s_nop 1
	v_writelane_b32 v254, s5, 51
	v_addc_co_u32_e64 v26, s[4:5], v39, v40, s[4:5]
	v_cmp_gt_u32_e64 s[4:5], v6, v7
	s_nop 1
	v_writelane_b32 v254, s4, 28
	s_nop 1
	v_writelane_b32 v254, s5, 29
	v_addc_co_u32_e64 v15, s[4:5], v25, v26, s[4:5]
	v_add3_u32 v15, v19, v20, v15
	v_add3_u32 v13, v13, v14, v15
	ds_bpermute_b32 v8, v8, v13
	v_cmp_eq_u32_e64 s[4:5], 0, v141
	s_waitcnt lgkmcnt(0)
	v_add_u32_e32 v8, v8, v13
	ds_bpermute_b32 v9, v9, v8
	s_waitcnt lgkmcnt(0)
	v_add_u32_e32 v8, v8, v9
	ds_bpermute_b32 v9, v10, v8
	v_mov_b32_e32 v10, s39
	s_waitcnt lgkmcnt(0)
	v_add_u32_e32 v8, v8, v9
	ds_bpermute_b32 v9, v11, v8
	v_mov_b32_e32 v11, s38
	v_cndmask_b32_e64 v10, v10, v11, s[4:5]
	s_waitcnt lgkmcnt(0)
	v_add_u32_e32 v8, v8, v9
	ds_bpermute_b32 v9, v12, v8
	s_waitcnt lgkmcnt(0)
	v_add_u32_e32 v8, v8, v9
	v_sub_u32_e32 v9, 0x100, v8
	v_lshlrev_b32_e64 v8, v1, -1
	v_bitop3_b32 v11, v10, v8, v10 bitop3:0x30
	v_bcnt_u32_b32 v11, v11, 0
	v_cmp_lt_i32_e32 vcc, v11, v9
	s_and_b64 s[38:39], s[38:39], vcc
	s_or_b64 s[38:39], s[36:37], s[38:39]
	v_cndmask_b32_e64 v11, 0, 1, s[38:39]
	v_cmp_ne_u32_e32 vcc, 0, v11
	v_not_b32_e32 v8, v8
	s_nop 0
	v_mov_b32_e32 v11, vcc_hi
	v_mov_b32_e32 v12, vcc_lo
	v_cndmask_b32_e64 v11, v11, v12, s[4:5]
	s_and_saveexec_b64 s[36:37], s[38:39]
	s_cbranch_execz .LBB0_2897
	v_and_b32_e32 v12, v11, v8
	v_bcnt_u32_b32 v12, v12, 0
	v_lshlrev_b32_e32 v86, 1, v12
	v_lshl_add_u64 v[12:13], v[4:5], 0, v[86:87]
	global_store_short v[12:13], v1, off
